# routing stage 1: counted LDS waits, each 16-score group is sorted as soon as its reads have landed
# speedup vs baseline: 1.0138x; 1.0062x over previous
; DI void routing_block(LAS unsigned char* lds, const bf16* q, const bf16* skb, int* experts, float* pgates, int tb) {
;     ...
;         const int t0 = tb * 32, hc = 8 * hp + wave;
;         f32x16 acc[4];
; #pragma unroll
;         for (int kb = 0; kb < 4; ++kb)
; #pragma unroll
;             for (int i = 0; i < 16; ++i) acc[kb][i] = 0.f;
; #pragma unroll
;         for (int ks = 0; ks < 8; ++ks) {
;             const bf16x8 a = *(const bf16x8*)(q + (size_t)(t0 + r) * QW + hc * 128 + 16 * ks + 8 * h);
; #pragma unroll
;             for (int kb = 0; kb < 4; ++kb) {
;                 const bf16x8 b = *(const bf16x8*)(skb + ((size_t)hc * 128 + 32 * kb + r) * 128 + 16 * ks + 8 * h);
;                 acc[kb] = __builtin_amdgcn_mfma_f32_32x32x16_bf16(a, b, acc[kb], 0, 0, 0);
;             }
;         }
.LBB0_894:
	s_lshl_b32 s76, s78, 3
	s_add_i32 s76, s76, s79
	s_lshl_b32 vcc_lo, s76, 7
	s_ashr_i32 vcc_hi, vcc_lo, 31
	v_lshl_add_u64 v[110:111], vcc, 1, v[80:81]
	s_ashr_i32 s77, s76, 31
	global_load_dwordx4 v[146:149], v[110:111], off
	global_load_dwordx4 v[150:153], v[110:111], off offset:32
	global_load_dwordx4 v[154:157], v[110:111], off offset:64
	global_load_dwordx4 v[158:161], v[110:111], off offset:96
	global_load_dwordx4 v[162:165], v[110:111], off offset:128
	global_load_dwordx4 v[166:169], v[110:111], off offset:160
	global_load_dwordx4 v[170:173], v[110:111], off offset:192
	global_load_dwordx4 v[174:177], v[110:111], off offset:224
	s_lshl_b64 s[76:77], s[76:77], 15
	v_mov_b32_e32 v105, s77
	v_or_b32_e32 v104, s76, v102
	v_lshl_add_u64 v[112:113], v[82:83], 0, v[104:105]
	v_or_b32_e32 v108, 0x2000, v104
	v_mov_b32_e32 v109, s77
	v_or_b32_e32 v106, 0x4000, v104
	v_mov_b32_e32 v107, s77
	v_or_b32_e32 v104, 0x6000, v104
	v_lshl_add_u64 v[242:243], v[82:83], 0, v[108:109]
	v_lshl_add_u64 v[244:245], v[82:83], 0, v[106:107]
	v_lshl_add_u64 v[246:247], v[82:83], 0, v[104:105]
	global_load_dwordx4 v[178:181], v[112:113], off
	global_load_dwordx4 v[182:185], v[242:243], off
	global_load_dwordx4 v[186:189], v[244:245], off
	global_load_dwordx4 v[190:193], v[246:247], off
	global_load_dwordx4 v[194:197], v[112:113], off offset:32
	global_load_dwordx4 v[198:201], v[242:243], off offset:32
	global_load_dwordx4 v[202:205], v[244:245], off offset:32
	global_load_dwordx4 v[206:209], v[246:247], off offset:32
	global_load_dwordx4 v[210:213], v[112:113], off offset:64
	global_load_dwordx4 v[214:217], v[242:243], off offset:64
	global_load_dwordx4 v[218:221], v[244:245], off offset:64
	global_load_dwordx4 v[222:225], v[246:247], off offset:64
	global_load_dwordx4 v[226:229], v[112:113], off offset:96
	global_load_dwordx4 v[230:233], v[242:243], off offset:96
	global_load_dwordx4 v[234:237], v[244:245], off offset:96
	global_load_dwordx4 v[238:241], v[246:247], off offset:96
	s_xor_b64 s[74:75], s[74:75], -1
	s_mov_b32 s76, 0
	s_waitcnt vmcnt(12)
	v_mfma_f32_32x32x16_bf16 v[50:65], v[146:149], v[178:181], 0
	v_mfma_f32_32x32x16_bf16 v[34:49], v[146:149], v[182:185], 0
	v_mfma_f32_32x32x16_bf16 v[18:33], v[146:149], v[186:189], 0
	v_mfma_f32_32x32x16_bf16 v[2:17], v[146:149], v[190:193], 0
	global_load_dwordx4 v[178:181], v[112:113], off offset:128
	global_load_dwordx4 v[182:185], v[242:243], off offset:128
	global_load_dwordx4 v[186:189], v[244:245], off offset:128
	global_load_dwordx4 v[190:193], v[246:247], off offset:128
	s_waitcnt vmcnt(12)
	v_mfma_f32_32x32x16_bf16 v[50:65], v[150:153], v[194:197], v[50:65]
	v_mfma_f32_32x32x16_bf16 v[34:49], v[150:153], v[198:201], v[34:49]
	v_mfma_f32_32x32x16_bf16 v[18:33], v[150:153], v[202:205], v[18:33]
	v_mfma_f32_32x32x16_bf16 v[2:17], v[150:153], v[206:209], v[2:17]
	global_load_dwordx4 v[194:197], v[112:113], off offset:160
	global_load_dwordx4 v[198:201], v[242:243], off offset:160
	global_load_dwordx4 v[202:205], v[244:245], off offset:160
	global_load_dwordx4 v[206:209], v[246:247], off offset:160
	s_waitcnt vmcnt(12)
	v_mfma_f32_32x32x16_bf16 v[50:65], v[154:157], v[210:213], v[50:65]
	v_mfma_f32_32x32x16_bf16 v[34:49], v[154:157], v[214:217], v[34:49]
	v_mfma_f32_32x32x16_bf16 v[18:33], v[154:157], v[218:221], v[18:33]
	v_mfma_f32_32x32x16_bf16 v[2:17], v[154:157], v[222:225], v[2:17]
	global_load_dwordx4 v[210:213], v[112:113], off offset:192
	global_load_dwordx4 v[214:217], v[242:243], off offset:192
	global_load_dwordx4 v[218:221], v[244:245], off offset:192
	global_load_dwordx4 v[222:225], v[246:247], off offset:192
	s_waitcnt vmcnt(12)
	v_mfma_f32_32x32x16_bf16 v[50:65], v[158:161], v[226:229], v[50:65]
	v_mfma_f32_32x32x16_bf16 v[34:49], v[158:161], v[230:233], v[34:49]
	v_mfma_f32_32x32x16_bf16 v[18:33], v[158:161], v[234:237], v[18:33]
	v_mfma_f32_32x32x16_bf16 v[2:17], v[158:161], v[238:241], v[2:17]
	global_load_dwordx4 v[226:229], v[112:113], off offset:224
	global_load_dwordx4 v[230:233], v[242:243], off offset:224
	global_load_dwordx4 v[234:237], v[244:245], off offset:224
	global_load_dwordx4 v[238:241], v[246:247], off offset:224
	s_waitcnt vmcnt(12)
	v_mfma_f32_32x32x16_bf16 v[50:65], v[162:165], v[178:181], v[50:65]
	v_mfma_f32_32x32x16_bf16 v[34:49], v[162:165], v[182:185], v[34:49]
	v_mfma_f32_32x32x16_bf16 v[18:33], v[162:165], v[186:189], v[18:33]
	v_mfma_f32_32x32x16_bf16 v[2:17], v[162:165], v[190:193], v[2:17]
	s_waitcnt vmcnt(8)
	v_mfma_f32_32x32x16_bf16 v[50:65], v[166:169], v[194:197], v[50:65]
	v_mfma_f32_32x32x16_bf16 v[34:49], v[166:169], v[198:201], v[34:49]
	v_mfma_f32_32x32x16_bf16 v[18:33], v[166:169], v[202:205], v[18:33]
	v_mfma_f32_32x32x16_bf16 v[2:17], v[166:169], v[206:209], v[2:17]
	s_waitcnt vmcnt(4)
	v_mfma_f32_32x32x16_bf16 v[50:65], v[170:173], v[210:213], v[50:65]
	v_mfma_f32_32x32x16_bf16 v[34:49], v[170:173], v[214:217], v[34:49]
	v_mfma_f32_32x32x16_bf16 v[18:33], v[170:173], v[218:221], v[18:33]
	v_mfma_f32_32x32x16_bf16 v[2:17], v[170:173], v[222:225], v[2:17]
	s_waitcnt vmcnt(0)
; DI int crow(int reg, int h) { return (reg & 3) + 8 * (reg >> 2) + 4 * h; }
; DI void routing_block(LAS unsigned char* lds, const bf16* q, const bf16* skb, int* experts, float* pgates, int tb) {
;     ...
;                 acc[kb] = __builtin_amdgcn_mfma_f32_32x32x16_bf16(a, b, acc[kb], 0, 0, 0);
;             }
;         }
; #pragma unroll
;         for (int kb = 0; kb < 4; ++kb)
; #pragma unroll
;             for (int i = 0; i < 16; ++i) {
;                 const int key = 32 * kb + r;
;                 sc[(crow(i, h) * 8 + wave) * RT_PITCH + key] = (f2key(acc[kb][i]) & ~127) | key;
;             }
	v_mfma_f32_32x32x16_bf16 v[50:65], v[174:177], v[226:229], v[50:65]
	v_mfma_f32_32x32x16_bf16 v[34:49], v[174:177], v[230:233], v[34:49]
	v_mfma_f32_32x32x16_bf16 v[18:33], v[174:177], v[234:237], v[18:33]
	v_mfma_f32_32x32x16_bf16 v[2:17], v[174:177], v[238:241], v[2:17]
	s_nop 11
	v_ashrrev_i32_e32 v105, 31, v51
	v_and_b32_e32 v105, 0x7fffff80, v105
	v_and_b32_e32 v51, 0xffffff80, v51
	v_bitop3_b32 v51, v105, v103, v51 bitop3:0xde
	v_ashrrev_i32_e32 v105, 31, v52
	v_and_b32_e32 v105, 0x7fffff80, v105
	v_and_b32_e32 v52, 0xffffff80, v52
	v_bitop3_b32 v52, v105, v103, v52 bitop3:0xde
	v_ashrrev_i32_e32 v105, 31, v53
	v_and_b32_e32 v105, 0x7fffff80, v105
	v_and_b32_e32 v53, 0xffffff80, v53
	v_bitop3_b32 v53, v105, v103, v53 bitop3:0xde
	v_ashrrev_i32_e32 v105, 31, v54
	v_and_b32_e32 v105, 0x7fffff80, v105
	v_and_b32_e32 v54, 0xffffff80, v54
	v_bitop3_b32 v54, v105, v103, v54 bitop3:0xde
	v_ashrrev_i32_e32 v105, 31, v55
	v_and_b32_e32 v105, 0x7fffff80, v105
	v_and_b32_e32 v55, 0xffffff80, v55
	v_bitop3_b32 v55, v105, v103, v55 bitop3:0xde
	v_ashrrev_i32_e32 v105, 31, v56
	v_and_b32_e32 v105, 0x7fffff80, v105
	v_and_b32_e32 v56, 0xffffff80, v56
	v_bitop3_b32 v56, v105, v103, v56 bitop3:0xde
	v_ashrrev_i32_e32 v105, 31, v57
	v_and_b32_e32 v105, 0x7fffff80, v105
	v_and_b32_e32 v57, 0xffffff80, v57
	v_bitop3_b32 v57, v105, v103, v57 bitop3:0xde
	v_ashrrev_i32_e32 v105, 31, v58
	v_and_b32_e32 v105, 0x7fffff80, v105
	v_and_b32_e32 v58, 0xffffff80, v58
	v_bitop3_b32 v58, v105, v103, v58 bitop3:0xde
	v_ashrrev_i32_e32 v105, 31, v59
	v_and_b32_e32 v105, 0x7fffff80, v105
	v_and_b32_e32 v59, 0xffffff80, v59
	v_bitop3_b32 v59, v105, v103, v59 bitop3:0xde
	v_ashrrev_i32_e32 v105, 31, v60
	v_and_b32_e32 v105, 0x7fffff80, v105
	v_and_b32_e32 v60, 0xffffff80, v60
	v_bitop3_b32 v60, v105, v103, v60 bitop3:0xde
	v_ashrrev_i32_e32 v105, 31, v61
	v_and_b32_e32 v105, 0x7fffff80, v105
	v_and_b32_e32 v61, 0xffffff80, v61
	v_bitop3_b32 v61, v105, v103, v61 bitop3:0xde
	v_ashrrev_i32_e32 v105, 31, v62
	v_and_b32_e32 v105, 0x7fffff80, v105
	v_and_b32_e32 v62, 0xffffff80, v62
	v_bitop3_b32 v62, v105, v103, v62 bitop3:0xde
	v_ashrrev_i32_e32 v105, 31, v63
	v_and_b32_e32 v105, 0x7fffff80, v105
	v_and_b32_e32 v63, 0xffffff80, v63
	v_bitop3_b32 v63, v105, v103, v63 bitop3:0xde
	v_ashrrev_i32_e32 v105, 31, v64
	v_and_b32_e32 v105, 0x7fffff80, v105
	v_and_b32_e32 v64, 0xffffff80, v64
	v_bitop3_b32 v64, v105, v103, v64 bitop3:0xde
	v_ashrrev_i32_e32 v105, 31, v65
	v_and_b32_e32 v105, 0x7fffff80, v105
	v_and_b32_e32 v65, 0xffffff80, v65
	v_ashrrev_i32_e32 v104, 31, v50
	v_bitop3_b32 v65, v105, v103, v65 bitop3:0xde
	v_ashrrev_i32_e32 v105, 31, v34
	v_and_b32_e32 v104, 0x7fffff80, v104
	v_and_b32_e32 v50, 0xffffff80, v50
	v_and_b32_e32 v105, 0x7fffff80, v105
	v_and_b32_e32 v34, 0xffffff80, v34
	v_bitop3_b32 v50, v104, v103, v50 bitop3:0xde
	v_add_u32_e32 v104, v123, v124
	v_bitop3_b32 v34, v105, v125, v34 bitop3:0xde
	ds_write2_b32 v104, v50, v34 offset1:32
	v_ashrrev_i32_e32 v34, 31, v35
	v_and_b32_e32 v34, 0x7fffff80, v34
	v_and_b32_e32 v35, 0xffffff80, v35
	v_bitop3_b32 v34, v34, v125, v35 bitop3:0xde
	v_add_u32_e32 v35, 0x1000, v104
	ds_write2_b32 v35, v51, v34 offset0:8 offset1:40
	v_ashrrev_i32_e32 v34, 31, v36
	v_and_b32_e32 v34, 0x7fffff80, v34
	v_and_b32_e32 v36, 0xffffff80, v36
	v_bitop3_b32 v34, v34, v125, v36 bitop3:0xde
	v_add_u32_e32 v36, 0x2000, v104
	ds_write2_b32 v36, v52, v34 offset0:16 offset1:48
	v_ashrrev_i32_e32 v34, 31, v37
	v_and_b32_e32 v34, 0x7fffff80, v34
	v_and_b32_e32 v37, 0xffffff80, v37
	v_bitop3_b32 v34, v34, v125, v37 bitop3:0xde
	v_add_u32_e32 v37, 0x3000, v104
	ds_write2_b32 v37, v53, v34 offset0:24 offset1:56
	v_ashrrev_i32_e32 v34, 31, v38
	v_and_b32_e32 v34, 0x7fffff80, v34
	v_and_b32_e32 v38, 0xffffff80, v38
	v_bitop3_b32 v34, v34, v125, v38 bitop3:0xde
	v_add_u32_e32 v38, 0x8000, v104
	ds_write2_b32 v38, v54, v34 offset0:64 offset1:96
	v_ashrrev_i32_e32 v34, 31, v39
	v_and_b32_e32 v34, 0x7fffff80, v34
	v_and_b32_e32 v39, 0xffffff80, v39
	v_bitop3_b32 v34, v34, v125, v39 bitop3:0xde
	v_add_u32_e32 v39, 0x9000, v104
	ds_write2_b32 v39, v55, v34 offset0:72 offset1:104
	v_ashrrev_i32_e32 v34, 31, v40
	v_and_b32_e32 v34, 0x7fffff80, v34
	v_and_b32_e32 v40, 0xffffff80, v40
	v_bitop3_b32 v34, v34, v125, v40 bitop3:0xde
	v_add_u32_e32 v40, 0xa000, v104
	ds_write2_b32 v40, v56, v34 offset0:80 offset1:112
	v_ashrrev_i32_e32 v34, 31, v41
	v_and_b32_e32 v34, 0x7fffff80, v34
	v_and_b32_e32 v41, 0xffffff80, v41
	v_bitop3_b32 v34, v34, v125, v41 bitop3:0xde
	v_add_u32_e32 v41, 0xb000, v104
	ds_write2_b32 v41, v57, v34 offset0:88 offset1:120
	v_ashrrev_i32_e32 v34, 31, v42
	v_and_b32_e32 v34, 0x7fffff80, v34
	v_and_b32_e32 v42, 0xffffff80, v42
	v_bitop3_b32 v34, v34, v125, v42 bitop3:0xde
	ds_write2_b32 v128, v58, v34 offset1:32
	v_ashrrev_i32_e32 v34, 31, v43
	v_and_b32_e32 v34, 0x7fffff80, v34
	v_and_b32_e32 v42, 0xffffff80, v43
	v_bitop3_b32 v34, v34, v125, v42 bitop3:0xde
	ds_write2_b32 v129, v59, v34 offset1:32
	v_ashrrev_i32_e32 v34, 31, v44
	v_and_b32_e32 v34, 0x7fffff80, v34
	v_and_b32_e32 v42, 0xffffff80, v44
	v_bitop3_b32 v34, v34, v125, v42 bitop3:0xde
	ds_write2_b32 v130, v60, v34 offset1:32
	v_ashrrev_i32_e32 v34, 31, v45
	v_and_b32_e32 v34, 0x7fffff80, v34
	v_and_b32_e32 v42, 0xffffff80, v45
	v_bitop3_b32 v34, v34, v125, v42 bitop3:0xde
	ds_write2_b32 v131, v61, v34 offset1:32
	v_ashrrev_i32_e32 v34, 31, v46
	v_and_b32_e32 v34, 0x7fffff80, v34
	v_and_b32_e32 v42, 0xffffff80, v46
	v_bitop3_b32 v34, v34, v125, v42 bitop3:0xde
	ds_write2_b32 v132, v62, v34 offset1:32
	v_ashrrev_i32_e32 v34, 31, v47
	v_and_b32_e32 v34, 0x7fffff80, v34
; DI int crow(int reg, int h) { return (reg & 3) + 8 * (reg >> 2) + 4 * h; }
; DI void routing_block(LAS unsigned char* lds, const bf16* q, const bf16* skb, int* experts, float* pgates, int tb) {
;     ...
; #pragma unroll
;         for (int kb = 0; kb < 4; ++kb)
; #pragma unroll
;             for (int i = 0; i < 16; ++i) {
;                 const int key = 32 * kb + r;
;                 sc[(crow(i, h) * 8 + wave) * RT_PITCH + key] = (f2key(acc[kb][i]) & ~127) | key;
;             }
;         __syncthreads();
	v_and_b32_e32 v42, 0xffffff80, v47
	v_bitop3_b32 v34, v34, v125, v42 bitop3:0xde
	ds_write2_b32 v133, v63, v34 offset1:32
	v_ashrrev_i32_e32 v34, 31, v48
	v_and_b32_e32 v34, 0x7fffff80, v34
	v_and_b32_e32 v42, 0xffffff80, v48
	v_bitop3_b32 v34, v34, v125, v42 bitop3:0xde
	ds_write2_b32 v134, v64, v34 offset1:32
	v_ashrrev_i32_e32 v34, 31, v49
	v_and_b32_e32 v34, 0x7fffff80, v34
	v_and_b32_e32 v42, 0xffffff80, v49
	v_bitop3_b32 v34, v34, v125, v42 bitop3:0xde
	ds_write2_b32 v135, v65, v34 offset1:32
	v_ashrrev_i32_e32 v34, 31, v18
	v_and_b32_e32 v34, 0x7fffff80, v34
	v_and_b32_e32 v18, 0xffffff80, v18
	v_bitop3_b32 v18, v34, v126, v18 bitop3:0xde
	v_ashrrev_i32_e32 v34, 31, v19
	v_and_b32_e32 v34, 0x7fffff80, v34
	v_and_b32_e32 v19, 0xffffff80, v19
	v_bitop3_b32 v19, v34, v126, v19 bitop3:0xde
	v_ashrrev_i32_e32 v34, 31, v20
	v_and_b32_e32 v34, 0x7fffff80, v34
	v_and_b32_e32 v20, 0xffffff80, v20
	v_bitop3_b32 v20, v34, v126, v20 bitop3:0xde
	v_ashrrev_i32_e32 v34, 31, v21
	v_and_b32_e32 v34, 0x7fffff80, v34
	v_and_b32_e32 v21, 0xffffff80, v21
	v_bitop3_b32 v21, v34, v126, v21 bitop3:0xde
	v_ashrrev_i32_e32 v34, 31, v22
	v_and_b32_e32 v34, 0x7fffff80, v34
	v_and_b32_e32 v22, 0xffffff80, v22
	v_bitop3_b32 v22, v34, v126, v22 bitop3:0xde
	v_ashrrev_i32_e32 v34, 31, v23
	v_and_b32_e32 v34, 0x7fffff80, v34
	v_and_b32_e32 v23, 0xffffff80, v23
	v_bitop3_b32 v23, v34, v126, v23 bitop3:0xde
	v_ashrrev_i32_e32 v34, 31, v24
	v_and_b32_e32 v34, 0x7fffff80, v34
	v_and_b32_e32 v24, 0xffffff80, v24
	v_bitop3_b32 v24, v34, v126, v24 bitop3:0xde
	v_ashrrev_i32_e32 v34, 31, v25
	v_and_b32_e32 v34, 0x7fffff80, v34
	v_and_b32_e32 v25, 0xffffff80, v25
	v_bitop3_b32 v25, v34, v126, v25 bitop3:0xde
	v_ashrrev_i32_e32 v34, 31, v26
	v_and_b32_e32 v34, 0x7fffff80, v34
	v_and_b32_e32 v26, 0xffffff80, v26
	v_bitop3_b32 v26, v34, v126, v26 bitop3:0xde
	v_ashrrev_i32_e32 v34, 31, v27
	v_and_b32_e32 v34, 0x7fffff80, v34
	v_and_b32_e32 v27, 0xffffff80, v27
	v_bitop3_b32 v27, v34, v126, v27 bitop3:0xde
	v_ashrrev_i32_e32 v34, 31, v28
	v_and_b32_e32 v34, 0x7fffff80, v34
	v_and_b32_e32 v28, 0xffffff80, v28
	v_bitop3_b32 v28, v34, v126, v28 bitop3:0xde
	v_ashrrev_i32_e32 v34, 31, v29
	v_and_b32_e32 v34, 0x7fffff80, v34
	v_and_b32_e32 v29, 0xffffff80, v29
	v_bitop3_b32 v29, v34, v126, v29 bitop3:0xde
	v_ashrrev_i32_e32 v34, 31, v30
	v_and_b32_e32 v34, 0x7fffff80, v34
	v_and_b32_e32 v30, 0xffffff80, v30
	v_bitop3_b32 v30, v34, v126, v30 bitop3:0xde
	v_ashrrev_i32_e32 v34, 31, v31
	v_and_b32_e32 v34, 0x7fffff80, v34
	v_and_b32_e32 v31, 0xffffff80, v31
	v_bitop3_b32 v31, v34, v126, v31 bitop3:0xde
	v_ashrrev_i32_e32 v34, 31, v32
	v_and_b32_e32 v34, 0x7fffff80, v34
	v_and_b32_e32 v32, 0xffffff80, v32
	v_bitop3_b32 v32, v34, v126, v32 bitop3:0xde
	v_ashrrev_i32_e32 v34, 31, v33
	v_and_b32_e32 v34, 0x7fffff80, v34
	v_and_b32_e32 v33, 0xffffff80, v33
	v_bitop3_b32 v33, v34, v126, v33 bitop3:0xde
	v_ashrrev_i32_e32 v34, 31, v2
	v_and_b32_e32 v34, 0x7fffff80, v34
	v_and_b32_e32 v2, 0xffffff80, v2
	v_bitop3_b32 v2, v34, v127, v2 bitop3:0xde
	ds_write2_b32 v104, v18, v2 offset0:64 offset1:96
	v_ashrrev_i32_e32 v2, 31, v3
	v_and_b32_e32 v2, 0x7fffff80, v2
	v_and_b32_e32 v3, 0xffffff80, v3
	v_bitop3_b32 v2, v2, v127, v3 bitop3:0xde
	ds_write2_b32 v35, v19, v2 offset0:72 offset1:104
	v_ashrrev_i32_e32 v2, 31, v4
	v_and_b32_e32 v2, 0x7fffff80, v2
	v_and_b32_e32 v3, 0xffffff80, v4
	v_bitop3_b32 v2, v2, v127, v3 bitop3:0xde
	ds_write2_b32 v36, v20, v2 offset0:80 offset1:112
	v_ashrrev_i32_e32 v2, 31, v5
	v_and_b32_e32 v2, 0x7fffff80, v2
	v_and_b32_e32 v3, 0xffffff80, v5
	v_bitop3_b32 v2, v2, v127, v3 bitop3:0xde
	ds_write2_b32 v37, v21, v2 offset0:88 offset1:120
	v_ashrrev_i32_e32 v2, 31, v6
	v_and_b32_e32 v2, 0x7fffff80, v2
	v_and_b32_e32 v3, 0xffffff80, v6
	v_bitop3_b32 v2, v2, v127, v3 bitop3:0xde
	ds_write2_b32 v38, v22, v2 offset0:128 offset1:160
	v_ashrrev_i32_e32 v2, 31, v7
	v_and_b32_e32 v2, 0x7fffff80, v2
	v_and_b32_e32 v3, 0xffffff80, v7
	v_bitop3_b32 v2, v2, v127, v3 bitop3:0xde
	ds_write2_b32 v39, v23, v2 offset0:136 offset1:168
	v_ashrrev_i32_e32 v2, 31, v8
	v_and_b32_e32 v2, 0x7fffff80, v2
	v_and_b32_e32 v3, 0xffffff80, v8
	v_bitop3_b32 v2, v2, v127, v3 bitop3:0xde
	ds_write2_b32 v40, v24, v2 offset0:144 offset1:176
	v_ashrrev_i32_e32 v2, 31, v9
	v_and_b32_e32 v2, 0x7fffff80, v2
	v_and_b32_e32 v3, 0xffffff80, v9
	v_bitop3_b32 v2, v2, v127, v3 bitop3:0xde
	ds_write2_b32 v41, v25, v2 offset0:152 offset1:184
	v_ashrrev_i32_e32 v2, 31, v10
	v_and_b32_e32 v2, 0x7fffff80, v2
	v_and_b32_e32 v3, 0xffffff80, v10
	v_bitop3_b32 v2, v2, v127, v3 bitop3:0xde
	ds_write2_b32 v128, v26, v2 offset0:64 offset1:96
	v_ashrrev_i32_e32 v2, 31, v11
	v_and_b32_e32 v2, 0x7fffff80, v2
	v_and_b32_e32 v3, 0xffffff80, v11
	v_bitop3_b32 v2, v2, v127, v3 bitop3:0xde
	ds_write2_b32 v129, v27, v2 offset0:64 offset1:96
	v_ashrrev_i32_e32 v2, 31, v12
	v_and_b32_e32 v2, 0x7fffff80, v2
	v_and_b32_e32 v3, 0xffffff80, v12
	v_bitop3_b32 v2, v2, v127, v3 bitop3:0xde
	ds_write2_b32 v130, v28, v2 offset0:64 offset1:96
	v_ashrrev_i32_e32 v2, 31, v13
	v_and_b32_e32 v2, 0x7fffff80, v2
	v_and_b32_e32 v3, 0xffffff80, v13
	v_bitop3_b32 v2, v2, v127, v3 bitop3:0xde
	ds_write2_b32 v131, v29, v2 offset0:64 offset1:96
	v_ashrrev_i32_e32 v2, 31, v14
	v_and_b32_e32 v2, 0x7fffff80, v2
	v_and_b32_e32 v3, 0xffffff80, v14
	v_bitop3_b32 v2, v2, v127, v3 bitop3:0xde
	ds_write2_b32 v132, v30, v2 offset0:64 offset1:96
	v_ashrrev_i32_e32 v2, 31, v15
	v_and_b32_e32 v2, 0x7fffff80, v2
	v_and_b32_e32 v3, 0xffffff80, v15
	v_bitop3_b32 v2, v2, v127, v3 bitop3:0xde
	ds_write2_b32 v133, v31, v2 offset0:64 offset1:96
	v_ashrrev_i32_e32 v2, 31, v16
	v_and_b32_e32 v2, 0x7fffff80, v2
	v_and_b32_e32 v3, 0xffffff80, v16
	v_bitop3_b32 v2, v2, v127, v3 bitop3:0xde
	ds_write2_b32 v134, v32, v2 offset0:64 offset1:96
	v_ashrrev_i32_e32 v2, 31, v17
	v_and_b32_e32 v2, 0x7fffff80, v2
	v_and_b32_e32 v3, 0xffffff80, v17
	v_bitop3_b32 v2, v2, v127, v3 bitop3:0xde
	ds_write2_b32 v135, v33, v2 offset0:64 offset1:96
	s_waitcnt lgkmcnt(0)
	s_barrier
; #define LAS __attribute__((address_space(3)))
; #define TOPK_INSERT(arr, xx) do { int _x = (xx); _Pragma("unroll") for (int _j = 0; _j < 16; ++_j) { const int _hi = max(arr[_j], _x); _x = min(arr[_j], _x); arr[_j] = _hi; } } while (0)
; DI void routing_block(LAS unsigned char* lds, const bf16* q, const bf16* skb, int* experts, float* pgates, int tb) {
;     ...
;             int a[16];
; #pragma unroll
;             for (int j = 0; j < 16; ++j) a[j] = (int)0x80000000;
;             LAS int* row = sc + (tid >> 1) * RT_PITCH; const int hf = tid & 1;
; #pragma unroll 8
;             for (int k = 0; k < 64; ++k) { const int x = row[64 * hf + k]; TOPK_INSERT(a, x); }
	ds_read2_b32 v[146:147], v120 offset0:0 offset1:1
	ds_read2_b32 v[148:149], v120 offset0:2 offset1:3
	ds_read2_b32 v[150:151], v120 offset0:4 offset1:5
	ds_read2_b32 v[152:153], v120 offset0:6 offset1:7
	ds_read2_b32 v[154:155], v120 offset0:8 offset1:9
	ds_read2_b32 v[156:157], v120 offset0:10 offset1:11
	ds_read2_b32 v[158:159], v120 offset0:12 offset1:13
	ds_read2_b32 v[160:161], v120 offset0:14 offset1:15
	ds_read2_b32 v[162:163], v120 offset0:16 offset1:17
	ds_read2_b32 v[164:165], v120 offset0:18 offset1:19
	ds_read2_b32 v[166:167], v120 offset0:20 offset1:21
	ds_read2_b32 v[168:169], v120 offset0:22 offset1:23
	ds_read2_b32 v[170:171], v120 offset0:24 offset1:25
	ds_read2_b32 v[172:173], v120 offset0:26 offset1:27
	ds_read2_b32 v[174:175], v120 offset0:28 offset1:29
	ds_read2_b32 v[176:177], v120 offset0:30 offset1:31
	ds_read2_b32 v[178:179], v120 offset0:32 offset1:33
	ds_read2_b32 v[180:181], v120 offset0:34 offset1:35
	ds_read2_b32 v[182:183], v120 offset0:36 offset1:37
	ds_read2_b32 v[184:185], v120 offset0:38 offset1:39
	ds_read2_b32 v[186:187], v120 offset0:40 offset1:41
	ds_read2_b32 v[188:189], v120 offset0:42 offset1:43
	ds_read2_b32 v[190:191], v120 offset0:44 offset1:45
	ds_read2_b32 v[192:193], v120 offset0:46 offset1:47
	ds_read2_b32 v[194:195], v120 offset0:48 offset1:49
	ds_read2_b32 v[196:197], v120 offset0:50 offset1:51
	ds_read2_b32 v[198:199], v120 offset0:52 offset1:53
	ds_read2_b32 v[200:201], v120 offset0:54 offset1:55
	ds_read2_b32 v[202:203], v120 offset0:56 offset1:57
	ds_read2_b32 v[204:205], v120 offset0:58 offset1:59
	ds_read2_b32 v[206:207], v120 offset0:60 offset1:61
	ds_read2_b32 v[208:209], v120 offset0:62 offset1:63
	s_waitcnt lgkmcnt(15)
	v_max_i32_e32 v18, v146, v147
	v_min_i32_e32 v147, v146, v147
	v_max_i32_e32 v19, v148, v149
	v_min_i32_e32 v149, v148, v149
	v_max_i32_e32 v20, v18, v19
	v_min_i32_e32 v19, v18, v19
	v_max_i32_e32 v21, v147, v149
	v_min_i32_e32 v149, v147, v149
	v_max_i32_e32 v146, v21, v19
	v_min_i32_e32 v19, v21, v19
	v_max_i32_e32 v148, v150, v151
	v_min_i32_e32 v151, v150, v151
	v_max_i32_e32 v18, v152, v153
	v_min_i32_e32 v153, v152, v153
	v_max_i32_e32 v147, v148, v18
	v_min_i32_e32 v18, v148, v18
	v_max_i32_e32 v21, v151, v153
	v_min_i32_e32 v153, v151, v153
	v_max_i32_e32 v150, v21, v18
	v_min_i32_e32 v18, v21, v18
	v_max_i32_e32 v152, v20, v147
	v_min_i32_e32 v147, v20, v147
	v_max_i32_e32 v148, v19, v18
	v_min_i32_e32 v18, v19, v18
	v_max_i32_e32 v151, v148, v147
	v_min_i32_e32 v147, v148, v147
	v_max_i32_e32 v21, v146, v150
	v_min_i32_e32 v150, v146, v150
	v_max_i32_e32 v20, v149, v153
	v_min_i32_e32 v153, v149, v153
	v_max_i32_e32 v19, v20, v150
	v_min_i32_e32 v150, v20, v150
	v_max_i32_e32 v148, v21, v151
	v_min_i32_e32 v151, v21, v151
	v_max_i32_e32 v146, v19, v147
	v_min_i32_e32 v147, v19, v147
	v_max_i32_e32 v149, v150, v18
	v_min_i32_e32 v18, v150, v18
	v_max_i32_e32 v20, v154, v155
	v_min_i32_e32 v155, v154, v155
	v_max_i32_e32 v21, v156, v157
	v_min_i32_e32 v157, v156, v157
	v_max_i32_e32 v19, v20, v21
	v_min_i32_e32 v21, v20, v21
	v_max_i32_e32 v150, v155, v157
	v_min_i32_e32 v157, v155, v157
	v_max_i32_e32 v154, v150, v21
	v_min_i32_e32 v21, v150, v21
	v_max_i32_e32 v156, v158, v159
	v_min_i32_e32 v159, v158, v159
	v_max_i32_e32 v20, v160, v161
	v_min_i32_e32 v161, v160, v161
	v_max_i32_e32 v155, v156, v20
	v_min_i32_e32 v20, v156, v20
	v_max_i32_e32 v150, v159, v161
	v_min_i32_e32 v161, v159, v161
	v_max_i32_e32 v158, v150, v20
	v_min_i32_e32 v20, v150, v20
	v_max_i32_e32 v160, v19, v155
	v_min_i32_e32 v155, v19, v155
	v_max_i32_e32 v156, v21, v20
	v_min_i32_e32 v20, v21, v20
	v_max_i32_e32 v159, v156, v155
	v_min_i32_e32 v155, v156, v155
	v_max_i32_e32 v150, v154, v158
	v_min_i32_e32 v158, v154, v158
	v_max_i32_e32 v19, v157, v161
	v_min_i32_e32 v161, v157, v161
	v_max_i32_e32 v21, v19, v158
	v_min_i32_e32 v158, v19, v158
	v_max_i32_e32 v156, v150, v159
	v_min_i32_e32 v159, v150, v159
	v_max_i32_e32 v154, v21, v155
	v_min_i32_e32 v155, v21, v155
	v_max_i32_e32 v157, v158, v20
	v_min_i32_e32 v20, v158, v20
	v_max_i32_e32 v19, v152, v160
	v_min_i32_e32 v160, v152, v160
	v_max_i32_e32 v150, v147, v155
	v_min_i32_e32 v155, v147, v155
	v_max_i32_e32 v21, v150, v160
	v_min_i32_e32 v160, v150, v160
	v_max_i32_e32 v158, v151, v159
	v_min_i32_e32 v159, v151, v159
	v_max_i32_e32 v152, v18, v20
	v_min_i32_e32 v20, v18, v20
	v_max_i32_e32 v147, v152, v159
	v_min_i32_e32 v159, v152, v159
	v_max_i32_e32 v150, v158, v21
	v_min_i32_e32 v21, v158, v21
	v_max_i32_e32 v151, v147, v160
	v_min_i32_e32 v160, v147, v160
	v_max_i32_e32 v18, v159, v155
	v_min_i32_e32 v155, v159, v155
	v_max_i32_e32 v152, v148, v156
	v_min_i32_e32 v156, v148, v156
	v_max_i32_e32 v158, v149, v157
	v_min_i32_e32 v157, v149, v157
	v_max_i32_e32 v147, v158, v156
	v_min_i32_e32 v156, v158, v156
	v_max_i32_e32 v159, v146, v154
	v_min_i32_e32 v154, v146, v154
	v_max_i32_e32 v148, v153, v161
	v_min_i32_e32 v161, v153, v161
	v_max_i32_e32 v149, v148, v154
	v_min_i32_e32 v154, v148, v154
	v_max_i32_e32 v158, v159, v147
	v_min_i32_e32 v147, v159, v147
	v_max_i32_e32 v146, v149, v156
	v_min_i32_e32 v156, v149, v156
	v_max_i32_e32 v153, v154, v157
	v_min_i32_e32 v157, v154, v157
	v_max_i32_e32 v148, v152, v150
	v_min_i32_e32 v150, v152, v150
	v_max_i32_e32 v159, v158, v21
	v_min_i32_e32 v21, v158, v21
	v_max_i32_e32 v149, v147, v151
	v_min_i32_e32 v151, v147, v151
	v_max_i32_e32 v154, v146, v160
	v_min_i32_e32 v160, v146, v160
	v_max_i32_e32 v152, v156, v18
	v_min_i32_e32 v18, v156, v18
	v_max_i32_e32 v158, v153, v155
	v_min_i32_e32 v155, v153, v155
	v_max_i32_e32 v147, v157, v20
	v_min_i32_e32 v20, v157, v20
	s_waitcnt lgkmcnt(15)
; #define LAS __attribute__((address_space(3)))
; #define TOPK_INSERT(arr, xx) do { int _x = (xx); _Pragma("unroll") for (int _j = 0; _j < 16; ++_j) { const int _hi = max(arr[_j], _x); _x = min(arr[_j], _x); arr[_j] = _hi; } } while (0)
; DI void routing_block(LAS unsigned char* lds, const bf16* q, const bf16* skb, int* experts, float* pgates, int tb) {
;     ...
;             int a[16];
; #pragma unroll
;             for (int j = 0; j < 16; ++j) a[j] = (int)0x80000000;
;             LAS int* row = sc + (tid >> 1) * RT_PITCH; const int hf = tid & 1;
; #pragma unroll 8
;             for (int k = 0; k < 64; ++k) { const int x = row[64 * hf + k]; TOPK_INSERT(a, x); }
	v_max_i32_e32 v146, v162, v163
	v_min_i32_e32 v163, v162, v163
	v_max_i32_e32 v156, v164, v165
	v_min_i32_e32 v165, v164, v165
	v_max_i32_e32 v153, v146, v156
	v_min_i32_e32 v156, v146, v156
	v_max_i32_e32 v157, v163, v165
	v_min_i32_e32 v165, v163, v165
	v_max_i32_e32 v162, v157, v156
	v_min_i32_e32 v156, v157, v156
	v_max_i32_e32 v164, v166, v167
	v_min_i32_e32 v167, v166, v167
	v_max_i32_e32 v146, v168, v169
	v_min_i32_e32 v169, v168, v169
	v_max_i32_e32 v163, v164, v146
	v_min_i32_e32 v146, v164, v146
	v_max_i32_e32 v157, v167, v169
	v_min_i32_e32 v169, v167, v169
	v_max_i32_e32 v166, v157, v146
	v_min_i32_e32 v146, v157, v146
	v_max_i32_e32 v168, v153, v163
	v_min_i32_e32 v163, v153, v163
	v_max_i32_e32 v164, v156, v146
	v_min_i32_e32 v146, v156, v146
	v_max_i32_e32 v167, v164, v163
	v_min_i32_e32 v163, v164, v163
	v_max_i32_e32 v157, v162, v166
	v_min_i32_e32 v166, v162, v166
	v_max_i32_e32 v153, v165, v169
	v_min_i32_e32 v169, v165, v169
	v_max_i32_e32 v156, v153, v166
	v_min_i32_e32 v166, v153, v166
	v_max_i32_e32 v164, v157, v167
	v_min_i32_e32 v167, v157, v167
	v_max_i32_e32 v162, v156, v163
	v_min_i32_e32 v163, v156, v163
	v_max_i32_e32 v165, v166, v146
	v_min_i32_e32 v146, v166, v146
	v_max_i32_e32 v153, v170, v171
	v_min_i32_e32 v171, v170, v171
	v_max_i32_e32 v157, v172, v173
	v_min_i32_e32 v173, v172, v173
	v_max_i32_e32 v156, v153, v157
	v_min_i32_e32 v157, v153, v157
	v_max_i32_e32 v166, v171, v173
	v_min_i32_e32 v173, v171, v173
	v_max_i32_e32 v170, v166, v157
	v_min_i32_e32 v157, v166, v157
	v_max_i32_e32 v172, v174, v175
	v_min_i32_e32 v175, v174, v175
	v_max_i32_e32 v153, v176, v177
	v_min_i32_e32 v177, v176, v177
	v_max_i32_e32 v171, v172, v153
	v_min_i32_e32 v153, v172, v153
	v_max_i32_e32 v166, v175, v177
	v_min_i32_e32 v177, v175, v177
	v_max_i32_e32 v174, v166, v153
	v_min_i32_e32 v153, v166, v153
	v_max_i32_e32 v176, v156, v171
	v_min_i32_e32 v171, v156, v171
	v_max_i32_e32 v172, v157, v153
	v_min_i32_e32 v153, v157, v153
	v_max_i32_e32 v175, v172, v171
	v_min_i32_e32 v171, v172, v171
	v_max_i32_e32 v166, v170, v174
	v_min_i32_e32 v174, v170, v174
	v_max_i32_e32 v156, v173, v177
	v_min_i32_e32 v177, v173, v177
	v_max_i32_e32 v157, v156, v174
	v_min_i32_e32 v174, v156, v174
	v_max_i32_e32 v172, v166, v175
	v_min_i32_e32 v175, v166, v175
	v_max_i32_e32 v170, v157, v171
	v_min_i32_e32 v171, v157, v171
	v_max_i32_e32 v173, v174, v153
	v_min_i32_e32 v153, v174, v153
	v_max_i32_e32 v156, v168, v176
	v_min_i32_e32 v176, v168, v176
	v_max_i32_e32 v166, v163, v171
	v_min_i32_e32 v171, v163, v171
	v_max_i32_e32 v157, v166, v176
	v_min_i32_e32 v176, v166, v176
	v_max_i32_e32 v174, v167, v175
	v_min_i32_e32 v175, v167, v175
	v_max_i32_e32 v168, v146, v153
	v_min_i32_e32 v153, v146, v153
	v_max_i32_e32 v163, v168, v175
	v_min_i32_e32 v175, v168, v175
	v_max_i32_e32 v166, v174, v157
	v_min_i32_e32 v157, v174, v157
	v_max_i32_e32 v167, v163, v176
	v_min_i32_e32 v176, v163, v176
	v_max_i32_e32 v146, v175, v171
	v_min_i32_e32 v171, v175, v171
	v_max_i32_e32 v168, v164, v172
	v_min_i32_e32 v172, v164, v172
	v_max_i32_e32 v174, v165, v173
	v_min_i32_e32 v173, v165, v173
	v_max_i32_e32 v163, v174, v172
	v_min_i32_e32 v172, v174, v172
	v_max_i32_e32 v175, v162, v170
	v_min_i32_e32 v170, v162, v170
	v_max_i32_e32 v164, v169, v177
	v_min_i32_e32 v177, v169, v177
	v_max_i32_e32 v165, v164, v170
	v_min_i32_e32 v170, v164, v170
	v_max_i32_e32 v174, v175, v163
	v_min_i32_e32 v163, v175, v163
	v_max_i32_e32 v162, v165, v172
	v_min_i32_e32 v172, v165, v172
	v_max_i32_e32 v169, v170, v173
	v_min_i32_e32 v173, v170, v173
	v_max_i32_e32 v164, v168, v166
	v_min_i32_e32 v166, v168, v166
	v_max_i32_e32 v175, v174, v157
	v_min_i32_e32 v157, v174, v157
	v_max_i32_e32 v165, v163, v167
	v_min_i32_e32 v167, v163, v167
	v_max_i32_e32 v170, v162, v176
	v_min_i32_e32 v176, v162, v176
	v_max_i32_e32 v168, v172, v146
	v_min_i32_e32 v146, v172, v146
	v_max_i32_e32 v174, v169, v171
	v_min_i32_e32 v171, v169, v171
	v_max_i32_e32 v163, v173, v153
	v_min_i32_e32 v153, v173, v153
	s_waitcnt lgkmcnt(8)
	v_max_i32_e32 v162, v178, v179
	v_min_i32_e32 v179, v178, v179
	v_max_i32_e32 v172, v180, v181
	v_min_i32_e32 v181, v180, v181
	v_max_i32_e32 v169, v162, v172
	v_min_i32_e32 v172, v162, v172
	v_max_i32_e32 v173, v179, v181
	v_min_i32_e32 v181, v179, v181
	v_max_i32_e32 v178, v173, v172
	v_min_i32_e32 v172, v173, v172
	v_max_i32_e32 v180, v182, v183
	v_min_i32_e32 v183, v182, v183
	v_max_i32_e32 v162, v184, v185
	v_min_i32_e32 v185, v184, v185
	v_max_i32_e32 v179, v180, v162
	v_min_i32_e32 v162, v180, v162
	v_max_i32_e32 v173, v183, v185
	v_min_i32_e32 v185, v183, v185
	v_max_i32_e32 v182, v173, v162
	v_min_i32_e32 v162, v173, v162
	v_max_i32_e32 v184, v169, v179
	v_min_i32_e32 v179, v169, v179
	v_max_i32_e32 v180, v172, v162
	v_min_i32_e32 v162, v172, v162
	v_max_i32_e32 v183, v180, v179
	v_min_i32_e32 v179, v180, v179
	v_max_i32_e32 v173, v178, v182
	v_min_i32_e32 v182, v178, v182
	v_max_i32_e32 v169, v181, v185
	v_min_i32_e32 v185, v181, v185
	v_max_i32_e32 v172, v169, v182
	v_min_i32_e32 v182, v169, v182
	v_max_i32_e32 v180, v173, v183
	v_min_i32_e32 v183, v173, v183
	v_max_i32_e32 v178, v172, v179
	v_min_i32_e32 v179, v172, v179
	v_max_i32_e32 v181, v182, v162
	v_min_i32_e32 v162, v182, v162
	v_max_i32_e32 v169, v186, v187
	v_min_i32_e32 v187, v186, v187
	v_max_i32_e32 v173, v188, v189
	v_min_i32_e32 v189, v188, v189
	v_max_i32_e32 v172, v169, v173
	v_min_i32_e32 v173, v169, v173
	v_max_i32_e32 v182, v187, v189
	v_min_i32_e32 v189, v187, v189
	v_max_i32_e32 v186, v182, v173
	v_min_i32_e32 v173, v182, v173
	v_max_i32_e32 v188, v190, v191
	v_min_i32_e32 v191, v190, v191
; #define LAS __attribute__((address_space(3)))
; #define TOPK_INSERT(arr, xx) do { int _x = (xx); _Pragma("unroll") for (int _j = 0; _j < 16; ++_j) { const int _hi = max(arr[_j], _x); _x = min(arr[_j], _x); arr[_j] = _hi; } } while (0)
; DI void routing_block(LAS unsigned char* lds, const bf16* q, const bf16* skb, int* experts, float* pgates, int tb) {
;     ...
;             int a[16];
; #pragma unroll
;             for (int j = 0; j < 16; ++j) a[j] = (int)0x80000000;
;             LAS int* row = sc + (tid >> 1) * RT_PITCH; const int hf = tid & 1;
; #pragma unroll 8
;             for (int k = 0; k < 64; ++k) { const int x = row[64 * hf + k]; TOPK_INSERT(a, x); }
	v_max_i32_e32 v169, v192, v193
	v_min_i32_e32 v193, v192, v193
	v_max_i32_e32 v187, v188, v169
	v_min_i32_e32 v169, v188, v169
	v_max_i32_e32 v182, v191, v193
	v_min_i32_e32 v193, v191, v193
	v_max_i32_e32 v190, v182, v169
	v_min_i32_e32 v169, v182, v169
	v_max_i32_e32 v192, v172, v187
	v_min_i32_e32 v187, v172, v187
	v_max_i32_e32 v188, v173, v169
	v_min_i32_e32 v169, v173, v169
	v_max_i32_e32 v191, v188, v187
	v_min_i32_e32 v187, v188, v187
	v_max_i32_e32 v182, v186, v190
	v_min_i32_e32 v190, v186, v190
	v_max_i32_e32 v172, v189, v193
	v_min_i32_e32 v193, v189, v193
	v_max_i32_e32 v173, v172, v190
	v_min_i32_e32 v190, v172, v190
	v_max_i32_e32 v188, v182, v191
	v_min_i32_e32 v191, v182, v191
	v_max_i32_e32 v186, v173, v187
	v_min_i32_e32 v187, v173, v187
	v_max_i32_e32 v189, v190, v169
	v_min_i32_e32 v169, v190, v169
	v_max_i32_e32 v172, v184, v192
	v_min_i32_e32 v192, v184, v192
	v_max_i32_e32 v182, v179, v187
	v_min_i32_e32 v187, v179, v187
	v_max_i32_e32 v173, v182, v192
	v_min_i32_e32 v192, v182, v192
	v_max_i32_e32 v190, v183, v191
	v_min_i32_e32 v191, v183, v191
	v_max_i32_e32 v184, v162, v169
	v_min_i32_e32 v169, v162, v169
	v_max_i32_e32 v179, v184, v191
	v_min_i32_e32 v191, v184, v191
	v_max_i32_e32 v182, v190, v173
	v_min_i32_e32 v173, v190, v173
	v_max_i32_e32 v183, v179, v192
	v_min_i32_e32 v192, v179, v192
	v_max_i32_e32 v162, v191, v187
	v_min_i32_e32 v187, v191, v187
	v_max_i32_e32 v184, v180, v188
	v_min_i32_e32 v188, v180, v188
	v_max_i32_e32 v190, v181, v189
	v_min_i32_e32 v189, v181, v189
	v_max_i32_e32 v179, v190, v188
	v_min_i32_e32 v188, v190, v188
	v_max_i32_e32 v191, v178, v186
	v_min_i32_e32 v186, v178, v186
	v_max_i32_e32 v180, v185, v193
	v_min_i32_e32 v193, v185, v193
	v_max_i32_e32 v181, v180, v186
	v_min_i32_e32 v186, v180, v186
	v_max_i32_e32 v190, v191, v179
	v_min_i32_e32 v179, v191, v179
	v_max_i32_e32 v178, v181, v188
	v_min_i32_e32 v188, v181, v188
	v_max_i32_e32 v185, v186, v189
	v_min_i32_e32 v189, v186, v189
	v_max_i32_e32 v180, v184, v182
	v_min_i32_e32 v182, v184, v182
	v_max_i32_e32 v191, v190, v173
	v_min_i32_e32 v173, v190, v173
	v_max_i32_e32 v181, v179, v183
	v_min_i32_e32 v183, v179, v183
	v_max_i32_e32 v186, v178, v192
	v_min_i32_e32 v192, v178, v192
	v_max_i32_e32 v184, v188, v162
	v_min_i32_e32 v162, v188, v162
	v_max_i32_e32 v190, v185, v187
	v_min_i32_e32 v187, v185, v187
	v_max_i32_e32 v179, v189, v169
	v_min_i32_e32 v169, v189, v169
	s_waitcnt lgkmcnt(0)
	v_max_i32_e32 v178, v194, v195
	v_min_i32_e32 v195, v194, v195
	v_max_i32_e32 v188, v196, v197
	v_min_i32_e32 v197, v196, v197
	v_max_i32_e32 v185, v178, v188
	v_min_i32_e32 v188, v178, v188
	v_max_i32_e32 v189, v195, v197
	v_min_i32_e32 v197, v195, v197
	v_max_i32_e32 v194, v189, v188
	v_min_i32_e32 v188, v189, v188
	v_max_i32_e32 v196, v198, v199
	v_min_i32_e32 v199, v198, v199
	v_max_i32_e32 v178, v200, v201
	v_min_i32_e32 v201, v200, v201
	v_max_i32_e32 v195, v196, v178
	v_min_i32_e32 v178, v196, v178
	v_max_i32_e32 v189, v199, v201
	v_min_i32_e32 v201, v199, v201
	v_max_i32_e32 v198, v189, v178
	v_min_i32_e32 v178, v189, v178
	v_max_i32_e32 v200, v185, v195
	v_min_i32_e32 v195, v185, v195
	v_max_i32_e32 v196, v188, v178
	v_min_i32_e32 v178, v188, v178
	v_max_i32_e32 v199, v196, v195
	v_min_i32_e32 v195, v196, v195
	v_max_i32_e32 v189, v194, v198
	v_min_i32_e32 v198, v194, v198
	v_max_i32_e32 v185, v197, v201
	v_min_i32_e32 v201, v197, v201
	v_max_i32_e32 v188, v185, v198
	v_min_i32_e32 v198, v185, v198
	v_max_i32_e32 v196, v189, v199
	v_min_i32_e32 v199, v189, v199
	v_max_i32_e32 v194, v188, v195
	v_min_i32_e32 v195, v188, v195
	v_max_i32_e32 v197, v198, v178
	v_min_i32_e32 v178, v198, v178
	v_max_i32_e32 v185, v202, v203
	v_min_i32_e32 v203, v202, v203
	v_max_i32_e32 v189, v204, v205
	v_min_i32_e32 v205, v204, v205
	v_max_i32_e32 v188, v185, v189
	v_min_i32_e32 v189, v185, v189
	v_max_i32_e32 v198, v203, v205
	v_min_i32_e32 v205, v203, v205
	v_max_i32_e32 v202, v198, v189
	v_min_i32_e32 v189, v198, v189
	v_max_i32_e32 v204, v206, v207
	v_min_i32_e32 v207, v206, v207
	v_max_i32_e32 v185, v208, v209
	v_min_i32_e32 v209, v208, v209
	v_max_i32_e32 v203, v204, v185
	v_min_i32_e32 v185, v204, v185
	v_max_i32_e32 v198, v207, v209
	v_min_i32_e32 v209, v207, v209
	v_max_i32_e32 v206, v198, v185
	v_min_i32_e32 v185, v198, v185
	v_max_i32_e32 v208, v188, v203
	v_min_i32_e32 v203, v188, v203
	v_max_i32_e32 v204, v189, v185
	v_min_i32_e32 v185, v189, v185
	v_max_i32_e32 v207, v204, v203
	v_min_i32_e32 v203, v204, v203
	v_max_i32_e32 v198, v202, v206
	v_min_i32_e32 v206, v202, v206
	v_max_i32_e32 v188, v205, v209
	v_min_i32_e32 v209, v205, v209
	v_max_i32_e32 v189, v188, v206
	v_min_i32_e32 v206, v188, v206
	v_max_i32_e32 v204, v198, v207
	v_min_i32_e32 v207, v198, v207
	v_max_i32_e32 v202, v189, v203
	v_min_i32_e32 v203, v189, v203
	v_max_i32_e32 v205, v206, v185
	v_min_i32_e32 v185, v206, v185
	v_max_i32_e32 v188, v200, v208
	v_min_i32_e32 v208, v200, v208
	v_max_i32_e32 v198, v195, v203
	v_min_i32_e32 v203, v195, v203
	v_max_i32_e32 v189, v198, v208
	v_min_i32_e32 v208, v198, v208
	v_max_i32_e32 v206, v199, v207
	v_min_i32_e32 v207, v199, v207
	v_max_i32_e32 v200, v178, v185
	v_min_i32_e32 v185, v178, v185
	v_max_i32_e32 v195, v200, v207
	v_min_i32_e32 v207, v200, v207
	v_max_i32_e32 v198, v206, v189
	v_min_i32_e32 v189, v206, v189
	v_max_i32_e32 v199, v195, v208
	v_min_i32_e32 v208, v195, v208
	v_max_i32_e32 v178, v207, v203
	v_min_i32_e32 v203, v207, v203
	v_max_i32_e32 v200, v196, v204
	v_min_i32_e32 v204, v196, v204
	v_max_i32_e32 v206, v197, v205
	v_min_i32_e32 v205, v197, v205
	v_max_i32_e32 v195, v206, v204
	v_min_i32_e32 v204, v206, v204
; #define LAS __attribute__((address_space(3)))
; #define TOPK_INSERT(arr, xx) do { int _x = (xx); _Pragma("unroll") for (int _j = 0; _j < 16; ++_j) { const int _hi = max(arr[_j], _x); _x = min(arr[_j], _x); arr[_j] = _hi; } } while (0)
; DI void routing_block(LAS unsigned char* lds, const bf16* q, const bf16* skb, int* experts, float* pgates, int tb) {
;     ...
;             int a[16];
; #pragma unroll
;             for (int j = 0; j < 16; ++j) a[j] = (int)0x80000000;
;             LAS int* row = sc + (tid >> 1) * RT_PITCH; const int hf = tid & 1;
; #pragma unroll 8
;             for (int k = 0; k < 64; ++k) { const int x = row[64 * hf + k]; TOPK_INSERT(a, x); }
;             __syncthreads();
; #pragma unroll
;             for (int j = 0; j < 16; ++j) row[16 * hf + j] = a[j];
;             __syncthreads();
;             if (hf == 0) {
; #pragma unroll
;                 for (int j = 0; j < 16; ++j) { const int x = row[16 + j]; TOPK_INSERT(a, x); }
	v_max_i32_e32 v207, v194, v202
	v_min_i32_e32 v202, v194, v202
	v_max_i32_e32 v196, v201, v209
	v_min_i32_e32 v209, v201, v209
	v_max_i32_e32 v197, v196, v202
	v_min_i32_e32 v202, v196, v202
	v_max_i32_e32 v206, v207, v195
	v_min_i32_e32 v195, v207, v195
	v_max_i32_e32 v194, v197, v204
	v_min_i32_e32 v204, v197, v204
	v_max_i32_e32 v201, v202, v205
	v_min_i32_e32 v205, v202, v205
	v_max_i32_e32 v196, v200, v198
	v_min_i32_e32 v198, v200, v198
	v_max_i32_e32 v207, v206, v189
	v_min_i32_e32 v189, v206, v189
	v_max_i32_e32 v197, v195, v199
	v_min_i32_e32 v199, v195, v199
	v_max_i32_e32 v202, v194, v208
	v_min_i32_e32 v208, v194, v208
	v_max_i32_e32 v200, v204, v178
	v_min_i32_e32 v178, v204, v178
	v_max_i32_e32 v206, v201, v203
	v_min_i32_e32 v203, v201, v203
	v_max_i32_e32 v195, v205, v185
	v_min_i32_e32 v185, v205, v185
	v_max_i32_e32 v19, v19, v177
	v_max_i32_e32 v148, v148, v153
	v_max_i32_e32 v150, v150, v163
	v_max_i32_e32 v159, v159, v171
	v_max_i32_e32 v21, v21, v174
	v_max_i32_e32 v149, v149, v146
	v_max_i32_e32 v151, v151, v168
	v_max_i32_e32 v154, v154, v176
	v_max_i32_e32 v160, v160, v170
	v_max_i32_e32 v152, v152, v167
	v_max_i32_e32 v18, v18, v165
	v_max_i32_e32 v158, v158, v157
	v_max_i32_e32 v155, v155, v175
	v_max_i32_e32 v147, v147, v166
	v_max_i32_e32 v20, v20, v164
	v_max_i32_e32 v161, v161, v156
	v_max_i32_e32 v194, v19, v160
	v_min_i32_e32 v160, v19, v160
	v_max_i32_e32 v204, v148, v152
	v_min_i32_e32 v152, v148, v152
	v_max_i32_e32 v201, v150, v18
	v_min_i32_e32 v18, v150, v18
	v_max_i32_e32 v205, v159, v158
	v_min_i32_e32 v158, v159, v158
	v_max_i32_e32 v156, v21, v155
	v_min_i32_e32 v155, v21, v155
	v_max_i32_e32 v164, v149, v147
	v_min_i32_e32 v147, v149, v147
	v_max_i32_e32 v166, v151, v20
	v_min_i32_e32 v20, v151, v20
	v_max_i32_e32 v175, v154, v161
	v_min_i32_e32 v161, v154, v161
	v_max_i32_e32 v157, v194, v156
	v_min_i32_e32 v156, v194, v156
	v_max_i32_e32 v165, v204, v164
	v_min_i32_e32 v164, v204, v164
	v_max_i32_e32 v167, v201, v166
	v_min_i32_e32 v166, v201, v166
	v_max_i32_e32 v170, v205, v175
	v_min_i32_e32 v175, v205, v175
	v_max_i32_e32 v176, v160, v155
	v_min_i32_e32 v155, v160, v155
	v_max_i32_e32 v168, v152, v147
	v_min_i32_e32 v147, v152, v147
	v_max_i32_e32 v146, v18, v20
	v_min_i32_e32 v20, v18, v20
	v_max_i32_e32 v174, v158, v161
	v_min_i32_e32 v161, v158, v161
	v_max_i32_e32 v171, v157, v167
	v_min_i32_e32 v167, v157, v167
	v_max_i32_e32 v163, v165, v170
	v_min_i32_e32 v170, v165, v170
	v_max_i32_e32 v153, v156, v166
	v_min_i32_e32 v166, v156, v166
	v_max_i32_e32 v177, v164, v175
	v_min_i32_e32 v175, v164, v175
	v_max_i32_e32 v19, v176, v146
	v_min_i32_e32 v146, v176, v146
	v_max_i32_e32 v148, v168, v174
	v_min_i32_e32 v174, v168, v174
	v_max_i32_e32 v150, v155, v20
	v_min_i32_e32 v20, v155, v20
	v_max_i32_e32 v159, v147, v161
	v_min_i32_e32 v161, v147, v161
	v_max_i32_e32 v21, v171, v163
	v_min_i32_e32 v163, v171, v163
	v_max_i32_e32 v149, v167, v170
	v_min_i32_e32 v170, v167, v170
	v_max_i32_e32 v151, v153, v177
	v_min_i32_e32 v177, v153, v177
	v_max_i32_e32 v154, v166, v175
	v_min_i32_e32 v175, v166, v175
	v_max_i32_e32 v194, v19, v148
	v_min_i32_e32 v148, v19, v148
	v_max_i32_e32 v204, v146, v174
	v_min_i32_e32 v174, v146, v174
	v_max_i32_e32 v201, v150, v159
	v_min_i32_e32 v159, v150, v159
	v_max_i32_e32 v205, v20, v161
	v_min_i32_e32 v161, v20, v161
	v_max_i32_e32 v172, v172, v209
	v_max_i32_e32 v180, v180, v185
	v_max_i32_e32 v182, v182, v195
	v_max_i32_e32 v191, v191, v203
	v_max_i32_e32 v173, v173, v206
	v_max_i32_e32 v181, v181, v178
	v_max_i32_e32 v183, v183, v200
	v_max_i32_e32 v186, v186, v208
	v_max_i32_e32 v192, v192, v202
	v_max_i32_e32 v184, v184, v199
	v_max_i32_e32 v162, v162, v197
	v_max_i32_e32 v190, v190, v189
	v_max_i32_e32 v187, v187, v207
	v_max_i32_e32 v179, v179, v198
	v_max_i32_e32 v169, v169, v196
	v_max_i32_e32 v193, v193, v188
	v_max_i32_e32 v160, v172, v192
	v_min_i32_e32 v192, v172, v192
	v_max_i32_e32 v152, v180, v184
	v_min_i32_e32 v184, v180, v184
	v_max_i32_e32 v18, v182, v162
	v_min_i32_e32 v162, v182, v162
	v_max_i32_e32 v158, v191, v190
	v_min_i32_e32 v190, v191, v190
	v_max_i32_e32 v157, v173, v187
	v_min_i32_e32 v187, v173, v187
	v_max_i32_e32 v165, v181, v179
	v_min_i32_e32 v179, v181, v179
	v_max_i32_e32 v156, v183, v169
	v_min_i32_e32 v169, v183, v169
	v_max_i32_e32 v164, v186, v193
	v_min_i32_e32 v193, v186, v193
	v_max_i32_e32 v176, v160, v157
	v_min_i32_e32 v157, v160, v157
	v_max_i32_e32 v168, v152, v165
	v_min_i32_e32 v165, v152, v165
	v_max_i32_e32 v155, v18, v156
	v_min_i32_e32 v156, v18, v156
	v_max_i32_e32 v147, v158, v164
	v_min_i32_e32 v164, v158, v164
	v_max_i32_e32 v171, v192, v187
	v_min_i32_e32 v187, v192, v187
	v_max_i32_e32 v167, v184, v179
	v_min_i32_e32 v179, v184, v179
	v_max_i32_e32 v153, v162, v169
	v_min_i32_e32 v169, v162, v169
	v_max_i32_e32 v166, v190, v193
	v_min_i32_e32 v193, v190, v193
	v_max_i32_e32 v19, v176, v155
	v_min_i32_e32 v155, v176, v155
	v_max_i32_e32 v146, v168, v147
	v_min_i32_e32 v147, v168, v147
	v_max_i32_e32 v150, v157, v156
	v_min_i32_e32 v156, v157, v156
	v_max_i32_e32 v20, v165, v164
	v_min_i32_e32 v164, v165, v164
	v_max_i32_e32 v188, v171, v153
	v_min_i32_e32 v153, v171, v153
	v_max_i32_e32 v196, v167, v166
	v_min_i32_e32 v166, v167, v166
	v_max_i32_e32 v198, v187, v169
	v_min_i32_e32 v169, v187, v169
	v_max_i32_e32 v207, v179, v193
	v_min_i32_e32 v193, v179, v193
	v_max_i32_e32 v189, v19, v146
	v_min_i32_e32 v146, v19, v146
	v_max_i32_e32 v197, v155, v147
	v_min_i32_e32 v147, v155, v147
	v_max_i32_e32 v199, v150, v20
	v_min_i32_e32 v20, v150, v20
	v_max_i32_e32 v202, v156, v164
	v_min_i32_e32 v164, v156, v164
; #define TOPK_INSERT(arr, xx) do { int _x = (xx); _Pragma("unroll") for (int _j = 0; _j < 16; ++_j) { const int _hi = max(arr[_j], _x); _x = min(arr[_j], _x); arr[_j] = _hi; } } while (0)
; DI void routing_block(LAS unsigned char* lds, const bf16* q, const bf16* skb, int* experts, float* pgates, int tb) {
;     ...
;             for (int k = 0; k < 64; ++k) { const int x = row[64 * hf + k]; TOPK_INSERT(a, x); }
;             __syncthreads();
; #pragma unroll
;             for (int j = 0; j < 16; ++j) row[16 * hf + j] = a[j];
;             __syncthreads();
;             if (hf == 0) {
; #pragma unroll
;                 for (int j = 0; j < 16; ++j) { const int x = row[16 + j]; TOPK_INSERT(a, x); }
; #pragma unroll
;                 for (int j = 0; j < 16; ++j) row[j] = a[j];
;             }
	v_max_i32_e32 v208, v188, v196
	v_min_i32_e32 v196, v188, v196
	v_max_i32_e32 v200, v153, v166
	v_min_i32_e32 v166, v153, v166
	v_max_i32_e32 v178, v198, v207
	v_min_i32_e32 v207, v198, v207
	v_max_i32_e32 v206, v169, v193
	v_min_i32_e32 v193, v169, v193
	v_max_i32_e32 v21, v21, v193
	v_max_i32_e32 v163, v163, v206
	v_max_i32_e32 v149, v149, v207
	v_max_i32_e32 v170, v170, v178
	v_max_i32_e32 v151, v151, v166
	v_max_i32_e32 v177, v177, v200
	v_max_i32_e32 v154, v154, v196
	v_max_i32_e32 v175, v175, v208
	v_max_i32_e32 v194, v194, v164
	v_max_i32_e32 v148, v148, v202
	v_max_i32_e32 v204, v204, v20
	v_max_i32_e32 v174, v174, v199
	v_max_i32_e32 v201, v201, v147
	v_max_i32_e32 v159, v159, v197
	v_max_i32_e32 v205, v205, v146
	v_max_i32_e32 v161, v161, v189
	v_max_i32_e32 v203, v21, v194
	v_min_i32_e32 v194, v21, v194
	v_max_i32_e32 v195, v163, v148
	v_min_i32_e32 v148, v163, v148
	v_max_i32_e32 v185, v149, v204
	v_min_i32_e32 v204, v149, v204
	v_max_i32_e32 v209, v170, v174
	v_min_i32_e32 v174, v170, v174
	v_max_i32_e32 v172, v151, v201
	v_min_i32_e32 v201, v151, v201
	v_max_i32_e32 v180, v177, v159
	v_min_i32_e32 v159, v177, v159
	v_max_i32_e32 v182, v154, v205
	v_min_i32_e32 v205, v154, v205
	v_max_i32_e32 v191, v175, v161
	v_min_i32_e32 v161, v175, v161
	v_max_i32_e32 v173, v203, v172
	v_min_i32_e32 v172, v203, v172
	v_max_i32_e32 v181, v195, v180
	v_min_i32_e32 v180, v195, v180
	v_max_i32_e32 v183, v185, v182
	v_min_i32_e32 v182, v185, v182
	v_max_i32_e32 v186, v209, v191
	v_min_i32_e32 v191, v209, v191
	v_max_i32_e32 v160, v194, v201
	v_min_i32_e32 v201, v194, v201
	v_max_i32_e32 v152, v148, v159
	v_min_i32_e32 v159, v148, v159
	v_max_i32_e32 v18, v204, v205
	v_min_i32_e32 v205, v204, v205
	v_max_i32_e32 v158, v174, v161
	v_min_i32_e32 v161, v174, v161
	v_max_i32_e32 v192, v173, v183
	v_min_i32_e32 v183, v173, v183
	v_max_i32_e32 v184, v181, v186
	v_min_i32_e32 v186, v181, v186
	v_max_i32_e32 v162, v172, v182
	v_min_i32_e32 v182, v172, v182
	v_max_i32_e32 v190, v180, v191
	v_min_i32_e32 v191, v180, v191
	v_max_i32_e32 v176, v160, v18
	v_min_i32_e32 v18, v160, v18
	v_max_i32_e32 v168, v152, v158
	v_min_i32_e32 v158, v152, v158
	v_max_i32_e32 v157, v201, v205
	v_min_i32_e32 v205, v201, v205
	v_max_i32_e32 v165, v159, v161
	v_min_i32_e32 v161, v159, v161
	v_max_i32_e32 v171, v192, v184
	v_min_i32_e32 v184, v192, v184
	v_max_i32_e32 v167, v183, v186
	v_min_i32_e32 v186, v183, v186
	v_max_i32_e32 v187, v162, v190
	v_min_i32_e32 v190, v162, v190
	v_max_i32_e32 v179, v182, v191
	v_min_i32_e32 v191, v182, v191
	v_max_i32_e32 v19, v176, v168
	v_min_i32_e32 v168, v176, v168
	v_max_i32_e32 v155, v18, v158
	v_min_i32_e32 v158, v18, v158
	v_max_i32_e32 v150, v157, v165
	v_min_i32_e32 v165, v157, v165
	v_max_i32_e32 v156, v205, v161
	v_min_i32_e32 v161, v205, v161
	s_nop 1
	v_mov_b32_dpp v34, v171 quad_perm:[1,0,3,2] row_mask:0xf bank_mask:0xf
	v_mov_b32_dpp v35, v184 quad_perm:[1,0,3,2] row_mask:0xf bank_mask:0xf
	v_mov_b32_dpp v36, v167 quad_perm:[1,0,3,2] row_mask:0xf bank_mask:0xf
	v_mov_b32_dpp v37, v186 quad_perm:[1,0,3,2] row_mask:0xf bank_mask:0xf
	v_mov_b32_dpp v38, v187 quad_perm:[1,0,3,2] row_mask:0xf bank_mask:0xf
	v_mov_b32_dpp v39, v190 quad_perm:[1,0,3,2] row_mask:0xf bank_mask:0xf
	v_mov_b32_dpp v40, v179 quad_perm:[1,0,3,2] row_mask:0xf bank_mask:0xf
	v_mov_b32_dpp v41, v191 quad_perm:[1,0,3,2] row_mask:0xf bank_mask:0xf
	v_mov_b32_dpp v42, v19 quad_perm:[1,0,3,2] row_mask:0xf bank_mask:0xf
	v_mov_b32_dpp v43, v168 quad_perm:[1,0,3,2] row_mask:0xf bank_mask:0xf
	v_mov_b32_dpp v44, v155 quad_perm:[1,0,3,2] row_mask:0xf bank_mask:0xf
	v_mov_b32_dpp v45, v158 quad_perm:[1,0,3,2] row_mask:0xf bank_mask:0xf
	v_mov_b32_dpp v46, v150 quad_perm:[1,0,3,2] row_mask:0xf bank_mask:0xf
	v_mov_b32_dpp v47, v165 quad_perm:[1,0,3,2] row_mask:0xf bank_mask:0xf
	v_mov_b32_dpp v48, v156 quad_perm:[1,0,3,2] row_mask:0xf bank_mask:0xf
	v_mov_b32_dpp v49, v161 quad_perm:[1,0,3,2] row_mask:0xf bank_mask:0xf
	v_max_i32_e32 v171, v171, v49
	v_max_i32_e32 v184, v184, v48
	v_max_i32_e32 v167, v167, v47
	v_max_i32_e32 v186, v186, v46
	v_max_i32_e32 v187, v187, v45
	v_max_i32_e32 v190, v190, v44
	v_max_i32_e32 v179, v179, v43
	v_max_i32_e32 v191, v191, v42
	v_max_i32_e32 v19, v19, v41
	v_max_i32_e32 v168, v168, v40
	v_max_i32_e32 v155, v155, v39
	v_max_i32_e32 v158, v158, v38
	v_max_i32_e32 v150, v150, v37
	v_max_i32_e32 v165, v165, v36
	v_max_i32_e32 v156, v156, v35
	v_max_i32_e32 v161, v161, v34
	v_max_i32_e32 v188, v171, v19
	v_min_i32_e32 v19, v171, v19
	v_max_i32_e32 v153, v184, v168
	v_min_i32_e32 v168, v184, v168
	v_max_i32_e32 v198, v167, v155
	v_min_i32_e32 v155, v167, v155
	v_max_i32_e32 v169, v186, v158
	v_min_i32_e32 v158, v186, v158
	v_max_i32_e32 v189, v187, v150
	v_min_i32_e32 v150, v187, v150
	v_max_i32_e32 v146, v190, v165
	v_min_i32_e32 v165, v190, v165
	v_max_i32_e32 v197, v179, v156
	v_min_i32_e32 v156, v179, v156
	v_max_i32_e32 v147, v191, v161
	v_min_i32_e32 v161, v191, v161
	v_max_i32_e32 v199, v188, v189
	v_min_i32_e32 v189, v188, v189
	v_max_i32_e32 v20, v153, v146
	v_min_i32_e32 v146, v153, v146
	v_max_i32_e32 v202, v198, v197
	v_min_i32_e32 v197, v198, v197
	v_max_i32_e32 v164, v169, v147
	v_min_i32_e32 v147, v169, v147
	v_max_i32_e32 v208, v19, v150
	v_min_i32_e32 v150, v19, v150
	v_max_i32_e32 v196, v168, v165
	v_min_i32_e32 v165, v168, v165
	v_max_i32_e32 v200, v155, v156
	v_min_i32_e32 v156, v155, v156
	v_max_i32_e32 v166, v158, v161
	v_min_i32_e32 v161, v158, v161
	v_max_i32_e32 v178, v199, v202
	v_min_i32_e32 v202, v199, v202
	v_max_i32_e32 v207, v20, v164
	v_min_i32_e32 v164, v20, v164
	v_max_i32_e32 v206, v189, v197
	v_min_i32_e32 v197, v189, v197
	v_max_i32_e32 v193, v146, v147
	v_min_i32_e32 v147, v146, v147
	v_max_i32_e32 v21, v208, v200
	v_min_i32_e32 v200, v208, v200
	v_max_i32_e32 v163, v196, v166
	v_min_i32_e32 v166, v196, v166
	v_max_i32_e32 v149, v150, v156
	v_min_i32_e32 v156, v150, v156
	v_max_i32_e32 v170, v165, v161
	v_min_i32_e32 v161, v165, v161
	v_max_i32_e32 v151, v178, v207
	v_min_i32_e32 v207, v178, v207
	v_max_i32_e32 v177, v202, v164
	v_min_i32_e32 v164, v202, v164
	v_max_i32_e32 v154, v206, v193
	v_min_i32_e32 v193, v206, v193
	v_max_i32_e32 v175, v197, v147
	v_min_i32_e32 v147, v197, v147
	v_max_i32_e32 v203, v21, v163
	v_min_i32_e32 v163, v21, v163
	v_max_i32_e32 v195, v200, v166
	v_min_i32_e32 v166, v200, v166
	v_max_i32_e32 v185, v149, v170
	v_min_i32_e32 v170, v149, v170
	v_max_i32_e32 v209, v156, v161
	v_min_i32_e32 v161, v156, v161
	s_and_saveexec_b64 s[76:77], s[44:45]
	s_cbranch_execz .LBB0_898
	ds_write2_b32 v119, v151, v207 offset0:0 offset1:1
	ds_write2_b32 v119, v177, v164 offset0:2 offset1:3
	ds_write2_b32 v119, v154, v193 offset0:4 offset1:5
	ds_write2_b32 v119, v175, v147 offset0:6 offset1:7
	ds_write2_b32 v119, v203, v163 offset0:8 offset1:9
	ds_write2_b32 v119, v195, v166 offset0:10 offset1:11
	ds_write2_b32 v119, v185, v170 offset0:12 offset1:13
	ds_write2_b32 v119, v209, v161 offset0:14 offset1:15
